# phase F row loop: touch loads for the wave's next latent row of X and O
# baseline (speedup 1.0000x reference)
.LBB0_801:
	s_min_i32 s7, s6, 0x2000
	s_lshr_b32 s7, s7, 12
	s_mulk_i32 s7, 0x6000
	v_add_u32_e32 v93, s7, v90
	s_ashr_i32 s7, s6, 31
	s_lshl_b64 s[12:13], s[6:7], 12
	v_lshl_add_u64 v[56:57], v[54:55], 0, s[12:13]
	ds_read_b128 v[24:27], v93
	ds_read_b128 v[28:31], v93 offset:16
	ds_read_b128 v[12:15], v93 offset:2048
	ds_read_b128 v[16:19], v93 offset:2064
	ds_read_b128 v[4:7], v93 offset:4096
	ds_read_b128 v[8:11], v93 offset:4112
	ds_read_b128 v[0:3], v93 offset:6144
	ds_read_b128 v[20:23], v93 offset:6160
	global_load_dwordx4 v[44:47], v[56:57], off
	global_load_dwordx4 v[40:43], v[56:57], off offset:1024
	global_load_dwordx4 v[36:39], v[56:57], off offset:2048
	global_load_dwordx4 v[32:35], v[56:57], off offset:3072
	v_lshl_add_u64 v[82:83], v[48:49], 0, s[12:13]
	global_load_dwordx4 v[62:65], v[82:83], off
	global_load_dwordx4 v[70:73], v[82:83], off offset:1024
	global_load_dwordx4 v[78:81], v[82:83], off offset:2048
	global_load_dwordx4 v[84:87], v[82:83], off offset:3072
	s_add_i32 s101, s6, s16
	s_cmpk_lt_i32 s101, 0x2000
	s_cselect_b32 s100, s101, s6
	s_lshl_b32 s100, s100, 12
	s_add_u32 s100, s100, 0x1ad00000
	s_add_u32 s100, s2, s100
	s_addc_u32 s101, s3, 0
	v_lshlrev_b32_e32 v106, 4, v144
	global_load_dword v107, v106, s[100:101]
	global_load_dword v107, v106, s[100:101] offset:1024
	global_load_dword v107, v106, s[100:101] offset:2048
	global_load_dword v107, v106, s[100:101] offset:3072
	s_add_u32 s100, s100, 0x6600000
	s_addc_u32 s101, s101, 0
	global_load_dword v107, v106, s[100:101]
	global_load_dword v107, v106, s[100:101] offset:1024
	global_load_dword v107, v106, s[100:101] offset:2048
	global_load_dword v107, v106, s[100:101] offset:3072
	s_and_b64 s[14:15], s[8:9], s[14:15]
	s_andn2_b64 vcc, exec, s[14:15]
	s_waitcnt vmcnt(11)
	v_lshlrev_b32_e32 v58, 16, v62
	v_and_b32_e32 v59, 0xffff0000, v62
	v_lshlrev_b32_e32 v60, 16, v63
	v_and_b32_e32 v61, 0xffff0000, v63
	v_lshlrev_b32_e32 v62, 16, v64
	v_and_b32_e32 v63, 0xffff0000, v64
	v_lshlrev_b32_e32 v64, 16, v65
	v_and_b32_e32 v65, 0xffff0000, v65
	s_waitcnt vmcnt(10)
	v_lshlrev_b32_e32 v66, 16, v70
	v_and_b32_e32 v67, 0xffff0000, v70
	v_lshlrev_b32_e32 v68, 16, v71
	v_and_b32_e32 v69, 0xffff0000, v71
	v_lshlrev_b32_e32 v70, 16, v72
	v_and_b32_e32 v71, 0xffff0000, v72
	v_lshlrev_b32_e32 v72, 16, v73
	v_and_b32_e32 v73, 0xffff0000, v73
	s_waitcnt vmcnt(9)
	v_lshlrev_b32_e32 v74, 16, v78
	v_and_b32_e32 v75, 0xffff0000, v78
	v_lshlrev_b32_e32 v76, 16, v79
	v_and_b32_e32 v77, 0xffff0000, v79
	v_lshlrev_b32_e32 v78, 16, v80
	v_and_b32_e32 v79, 0xffff0000, v80
	v_lshlrev_b32_e32 v80, 16, v81
	v_and_b32_e32 v81, 0xffff0000, v81
	s_waitcnt vmcnt(8)
	v_lshlrev_b32_e32 v82, 16, v84
	v_and_b32_e32 v83, 0xffff0000, v84
	v_lshlrev_b32_e32 v84, 16, v85
	v_and_b32_e32 v85, 0xffff0000, v85
	v_lshlrev_b32_e32 v88, 16, v86
	v_and_b32_e32 v89, 0xffff0000, v86
	v_lshlrev_b32_e32 v86, 16, v87
	v_and_b32_e32 v87, 0xffff0000, v87
	s_cbranch_vccnz .LBB0_794
	s_add_i32 s28, s6, 0xffffe000
	s_lshl_b64 s[14:15], s[28:29], 12
	v_lshl_add_u64 v[100:101], v[50:51], 0, s[14:15]
	global_load_dwordx4 v[94:97], v[100:101], off
	s_waitcnt vmcnt(0)
	v_lshlrev_b32_e32 v102, 16, v94
	v_and_b32_e32 v103, 0xffff0000, v94
	v_lshlrev_b32_e32 v94, 16, v95
	v_and_b32_e32 v95, 0xffff0000, v95
	v_lshlrev_b32_e32 v110, 16, v96
	v_and_b32_e32 v111, 0xffff0000, v96
	v_lshlrev_b32_e32 v96, 16, v97
	v_and_b32_e32 v97, 0xffff0000, v97
	v_pk_add_f32 v[60:61], v[60:61], v[94:95]
	v_pk_add_f32 v[64:65], v[64:65], v[96:97]
	global_load_dwordx4 v[94:97], v[100:101], off offset:1024
	v_pk_add_f32 v[58:59], v[58:59], v[102:103]
	v_pk_add_f32 v[62:63], v[62:63], v[110:111]
	s_waitcnt vmcnt(0)
	v_lshlrev_b32_e32 v102, 16, v94
	v_and_b32_e32 v103, 0xffff0000, v94
	v_lshlrev_b32_e32 v94, 16, v95
	v_and_b32_e32 v95, 0xffff0000, v95
	v_lshlrev_b32_e32 v110, 16, v96
	v_and_b32_e32 v111, 0xffff0000, v96
	v_lshlrev_b32_e32 v96, 16, v97
	v_and_b32_e32 v97, 0xffff0000, v97
	v_pk_add_f32 v[68:69], v[68:69], v[94:95]
	v_pk_add_f32 v[72:73], v[72:73], v[96:97]
	global_load_dwordx4 v[94:97], v[100:101], off offset:2048
	v_pk_add_f32 v[66:67], v[66:67], v[102:103]
	v_pk_add_f32 v[70:71], v[70:71], v[110:111]
	s_waitcnt vmcnt(0)
	v_lshlrev_b32_e32 v102, 16, v94
	v_and_b32_e32 v103, 0xffff0000, v94
	v_lshlrev_b32_e32 v94, 16, v95
	v_and_b32_e32 v95, 0xffff0000, v95
	v_lshlrev_b32_e32 v110, 16, v96
	v_and_b32_e32 v111, 0xffff0000, v96
	v_lshlrev_b32_e32 v96, 16, v97
	v_and_b32_e32 v97, 0xffff0000, v97
	v_pk_add_f32 v[76:77], v[76:77], v[94:95]
	v_pk_add_f32 v[80:81], v[80:81], v[96:97]
	global_load_dwordx4 v[94:97], v[100:101], off offset:3072
	v_pk_add_f32 v[74:75], v[74:75], v[102:103]
	v_pk_add_f32 v[78:79], v[78:79], v[110:111]
	s_waitcnt vmcnt(0)
	v_lshlrev_b32_e32 v100, 16, v94
	v_and_b32_e32 v101, 0xffff0000, v94
	v_lshlrev_b32_e32 v94, 16, v95
	v_and_b32_e32 v95, 0xffff0000, v95
	v_lshlrev_b32_e32 v102, 16, v96
	v_and_b32_e32 v103, 0xffff0000, v96
	v_lshlrev_b32_e32 v96, 16, v97
	v_and_b32_e32 v97, 0xffff0000, v97
	v_pk_add_f32 v[82:83], v[82:83], v[100:101]
	v_pk_add_f32 v[84:85], v[84:85], v[94:95]
	v_pk_add_f32 v[88:89], v[88:89], v[102:103]
	v_pk_add_f32 v[86:87], v[86:87], v[96:97]
	s_branch .LBB0_794
